# adds: modulation-vector GEMV with 64 weight loads in flight
# speedup vs baseline: 1.0165x; 1.0005x over previous
;     ...
;         const int jj = tid & 63, ks = tid >> 6;
;         const float* w = P.in[4] + (size_t)layer * 1024 * 6144 + j0 + jj;
;         float a0 = 0.f, a1 = 0.f;
; #pragma unroll 8
;         for (int k = ks * 128; k < ks * 128 + 128; ++k) { const float wv = w[(size_t)k * 6144]; a0 += sv[k] * wv; a1 += sv[1024 + k] * wv; }
;         red[(ks * 64 + jj) * 2] = a0; red[(ks * 64 + jj) * 2 + 1] = a1;
.LBB0_12:
	v_readlane_b32 s98, v253, 27
	v_readlane_b32 s99, v253, 28
	s_add_u32 s98, s98, s0
	s_addc_u32 s99, s99, s1
	v_mul_u32_u24_e32 v34, 0x300000, v1
	v_lshl_or_b32 v34, v202, 2, v34
	global_load_dword v66, v34, s[98:99]
	s_add_u32 s98, s98, 0x6000
	s_addc_u32 s99, s99, 0
	global_load_dword v67, v34, s[98:99]
	s_add_u32 s98, s98, 0x6000
	s_addc_u32 s99, s99, 0
	global_load_dword v68, v34, s[98:99]
	s_add_u32 s98, s98, 0x6000
	s_addc_u32 s99, s99, 0
	global_load_dword v69, v34, s[98:99]
	s_add_u32 s98, s98, 0x6000
	s_addc_u32 s99, s99, 0
	global_load_dword v70, v34, s[98:99]
	s_add_u32 s98, s98, 0x6000
	s_addc_u32 s99, s99, 0
	global_load_dword v71, v34, s[98:99]
	s_add_u32 s98, s98, 0x6000
	s_addc_u32 s99, s99, 0
	global_load_dword v72, v34, s[98:99]
	s_add_u32 s98, s98, 0x6000
	s_addc_u32 s99, s99, 0
	global_load_dword v73, v34, s[98:99]
	s_add_u32 s98, s98, 0x6000
	s_addc_u32 s99, s99, 0
	global_load_dword v74, v34, s[98:99]
	s_add_u32 s98, s98, 0x6000
	s_addc_u32 s99, s99, 0
	global_load_dword v75, v34, s[98:99]
	s_add_u32 s98, s98, 0x6000
	s_addc_u32 s99, s99, 0
	global_load_dword v76, v34, s[98:99]
	s_add_u32 s98, s98, 0x6000
	s_addc_u32 s99, s99, 0
	global_load_dword v77, v34, s[98:99]
	s_add_u32 s98, s98, 0x6000
	s_addc_u32 s99, s99, 0
	global_load_dword v78, v34, s[98:99]
	s_add_u32 s98, s98, 0x6000
	s_addc_u32 s99, s99, 0
	global_load_dword v79, v34, s[98:99]
	s_add_u32 s98, s98, 0x6000
	s_addc_u32 s99, s99, 0
	global_load_dword v80, v34, s[98:99]
	s_add_u32 s98, s98, 0x6000
	s_addc_u32 s99, s99, 0
	global_load_dword v81, v34, s[98:99]
	s_add_u32 s98, s98, 0x6000
	s_addc_u32 s99, s99, 0
	global_load_dword v82, v34, s[98:99]
	s_add_u32 s98, s98, 0x6000
	s_addc_u32 s99, s99, 0
	global_load_dword v83, v34, s[98:99]
	s_add_u32 s98, s98, 0x6000
	s_addc_u32 s99, s99, 0
	global_load_dword v84, v34, s[98:99]
	s_add_u32 s98, s98, 0x6000
	s_addc_u32 s99, s99, 0
	global_load_dword v85, v34, s[98:99]
	s_add_u32 s98, s98, 0x6000
	s_addc_u32 s99, s99, 0
	global_load_dword v86, v34, s[98:99]
	s_add_u32 s98, s98, 0x6000
	s_addc_u32 s99, s99, 0
	global_load_dword v87, v34, s[98:99]
	s_add_u32 s98, s98, 0x6000
	s_addc_u32 s99, s99, 0
	global_load_dword v88, v34, s[98:99]
	s_add_u32 s98, s98, 0x6000
	s_addc_u32 s99, s99, 0
	global_load_dword v89, v34, s[98:99]
	s_add_u32 s98, s98, 0x6000
	s_addc_u32 s99, s99, 0
	global_load_dword v90, v34, s[98:99]
	s_add_u32 s98, s98, 0x6000
	s_addc_u32 s99, s99, 0
	global_load_dword v91, v34, s[98:99]
	s_add_u32 s98, s98, 0x6000
	s_addc_u32 s99, s99, 0
	global_load_dword v92, v34, s[98:99]
	s_add_u32 s98, s98, 0x6000
	s_addc_u32 s99, s99, 0
	global_load_dword v93, v34, s[98:99]
	s_add_u32 s98, s98, 0x6000
	s_addc_u32 s99, s99, 0
	global_load_dword v94, v34, s[98:99]
	s_add_u32 s98, s98, 0x6000
	s_addc_u32 s99, s99, 0
	global_load_dword v95, v34, s[98:99]
	s_add_u32 s98, s98, 0x6000
	s_addc_u32 s99, s99, 0
	global_load_dword v96, v34, s[98:99]
	s_add_u32 s98, s98, 0x6000
	s_addc_u32 s99, s99, 0
	global_load_dword v97, v34, s[98:99]
	s_add_u32 s98, s98, 0x6000
	s_addc_u32 s99, s99, 0
	global_load_dword v98, v34, s[98:99]
	s_add_u32 s98, s98, 0x6000
	s_addc_u32 s99, s99, 0
	global_load_dword v99, v34, s[98:99]
	s_add_u32 s98, s98, 0x6000
	s_addc_u32 s99, s99, 0
	global_load_dword v100, v34, s[98:99]
	s_add_u32 s98, s98, 0x6000
	s_addc_u32 s99, s99, 0
	global_load_dword v101, v34, s[98:99]
	s_add_u32 s98, s98, 0x6000
	s_addc_u32 s99, s99, 0
	global_load_dword v102, v34, s[98:99]
	s_add_u32 s98, s98, 0x6000
	s_addc_u32 s99, s99, 0
	global_load_dword v103, v34, s[98:99]
	s_add_u32 s98, s98, 0x6000
	s_addc_u32 s99, s99, 0
	global_load_dword v104, v34, s[98:99]
	s_add_u32 s98, s98, 0x6000
	s_addc_u32 s99, s99, 0
	global_load_dword v105, v34, s[98:99]
	s_add_u32 s98, s98, 0x6000
	s_addc_u32 s99, s99, 0
	global_load_dword v106, v34, s[98:99]
	s_add_u32 s98, s98, 0x6000
	s_addc_u32 s99, s99, 0
	global_load_dword v107, v34, s[98:99]
	s_add_u32 s98, s98, 0x6000
	s_addc_u32 s99, s99, 0
	global_load_dword v108, v34, s[98:99]
	s_add_u32 s98, s98, 0x6000
	s_addc_u32 s99, s99, 0
	global_load_dword v109, v34, s[98:99]
	s_add_u32 s98, s98, 0x6000
	s_addc_u32 s99, s99, 0
	global_load_dword v110, v34, s[98:99]
	s_add_u32 s98, s98, 0x6000
	s_addc_u32 s99, s99, 0
	global_load_dword v111, v34, s[98:99]
	s_add_u32 s98, s98, 0x6000
	s_addc_u32 s99, s99, 0
	global_load_dword v112, v34, s[98:99]
	s_add_u32 s98, s98, 0x6000
	s_addc_u32 s99, s99, 0
	global_load_dword v113, v34, s[98:99]
	s_add_u32 s98, s98, 0x6000
	s_addc_u32 s99, s99, 0
	global_load_dword v114, v34, s[98:99]
	s_add_u32 s98, s98, 0x6000
	s_addc_u32 s99, s99, 0
	global_load_dword v115, v34, s[98:99]
	s_add_u32 s98, s98, 0x6000
	s_addc_u32 s99, s99, 0
	global_load_dword v116, v34, s[98:99]
	s_add_u32 s98, s98, 0x6000
	s_addc_u32 s99, s99, 0
	global_load_dword v117, v34, s[98:99]
	s_add_u32 s98, s98, 0x6000
	s_addc_u32 s99, s99, 0
	global_load_dword v118, v34, s[98:99]
	s_add_u32 s98, s98, 0x6000
	s_addc_u32 s99, s99, 0
	global_load_dword v119, v34, s[98:99]
	s_add_u32 s98, s98, 0x6000
	s_addc_u32 s99, s99, 0
	global_load_dword v120, v34, s[98:99]
	s_add_u32 s98, s98, 0x6000
	s_addc_u32 s99, s99, 0
	global_load_dword v121, v34, s[98:99]
	s_add_u32 s98, s98, 0x6000
	s_addc_u32 s99, s99, 0
	global_load_dword v122, v34, s[98:99]
	s_add_u32 s98, s98, 0x6000
	s_addc_u32 s99, s99, 0
	global_load_dword v123, v34, s[98:99]
	s_add_u32 s98, s98, 0x6000
	s_addc_u32 s99, s99, 0
	global_load_dword v124, v34, s[98:99]
	s_add_u32 s98, s98, 0x6000
	s_addc_u32 s99, s99, 0
	global_load_dword v125, v34, s[98:99]
	s_add_u32 s98, s98, 0x6000
	s_addc_u32 s99, s99, 0
	global_load_dword v126, v34, s[98:99]
	s_add_u32 s98, s98, 0x6000
	s_addc_u32 s99, s99, 0
	global_load_dword v127, v34, s[98:99]
	s_add_u32 s98, s98, 0x6000
	s_addc_u32 s99, s99, 0
	global_load_dword v128, v34, s[98:99]
	s_add_u32 s98, s98, 0x6000
	s_addc_u32 s99, s99, 0
	global_load_dword v129, v34, s[98:99]
	s_add_u32 s98, s98, 0x6000
	s_addc_u32 s99, s99, 0
	ds_read_b128 v[18:21], v2 offset:0
	ds_read_b128 v[22:25], v2 offset:16
	ds_read_b128 v[26:29], v2 offset:4096
	ds_read_b128 v[30:33], v2 offset:4112
	s_waitcnt vmcnt(56) lgkmcnt(0)
;     ...
; #pragma unroll 8
;         for (int k = ks * 128; k < ks * 128 + 128; ++k) { const float wv = w[(size_t)k * 6144]; a0 += sv[k] * wv; a1 += sv[1024 + k] * wv; }
	v_fmac_f32_e32 v12, v66, v18
	v_fmac_f32_e32 v13, v66, v26
	v_fmac_f32_e32 v12, v67, v19
	v_fmac_f32_e32 v13, v67, v27
	v_fmac_f32_e32 v12, v68, v20
	v_fmac_f32_e32 v13, v68, v28
	v_fmac_f32_e32 v12, v69, v21
	v_fmac_f32_e32 v13, v69, v29
	v_fmac_f32_e32 v12, v70, v22
	v_fmac_f32_e32 v13, v70, v30
	v_fmac_f32_e32 v12, v71, v23
	v_fmac_f32_e32 v13, v71, v31
	v_fmac_f32_e32 v12, v72, v24
	v_fmac_f32_e32 v13, v72, v32
	v_fmac_f32_e32 v12, v73, v25
	v_fmac_f32_e32 v13, v73, v33
	global_load_dword v130, v34, s[98:99]
	s_add_u32 s98, s98, 0x6000
	s_addc_u32 s99, s99, 0
	global_load_dword v131, v34, s[98:99]
	s_add_u32 s98, s98, 0x6000
	s_addc_u32 s99, s99, 0
	global_load_dword v132, v34, s[98:99]
	s_add_u32 s98, s98, 0x6000
	s_addc_u32 s99, s99, 0
	global_load_dword v133, v34, s[98:99]
	s_add_u32 s98, s98, 0x6000
	s_addc_u32 s99, s99, 0
	global_load_dword v134, v34, s[98:99]
	s_add_u32 s98, s98, 0x6000
	s_addc_u32 s99, s99, 0
	global_load_dword v135, v34, s[98:99]
	s_add_u32 s98, s98, 0x6000
	s_addc_u32 s99, s99, 0
	global_load_dword v136, v34, s[98:99]
	s_add_u32 s98, s98, 0x6000
	s_addc_u32 s99, s99, 0
	global_load_dword v137, v34, s[98:99]
	s_add_u32 s98, s98, 0x6000
	s_addc_u32 s99, s99, 0
	ds_read_b128 v[18:21], v2 offset:32
	ds_read_b128 v[22:25], v2 offset:48
	ds_read_b128 v[26:29], v2 offset:4128
	ds_read_b128 v[30:33], v2 offset:4144
	s_waitcnt vmcnt(56) lgkmcnt(0)
	v_fmac_f32_e32 v12, v74, v18
	v_fmac_f32_e32 v13, v74, v26
	v_fmac_f32_e32 v12, v75, v19
	v_fmac_f32_e32 v13, v75, v27
	v_fmac_f32_e32 v12, v76, v20
	v_fmac_f32_e32 v13, v76, v28
	v_fmac_f32_e32 v12, v77, v21
	v_fmac_f32_e32 v13, v77, v29
	v_fmac_f32_e32 v12, v78, v22
	v_fmac_f32_e32 v13, v78, v30
	v_fmac_f32_e32 v12, v79, v23
	v_fmac_f32_e32 v13, v79, v31
	v_fmac_f32_e32 v12, v80, v24
	v_fmac_f32_e32 v13, v80, v32
	v_fmac_f32_e32 v12, v81, v25
	v_fmac_f32_e32 v13, v81, v33
	global_load_dword v138, v34, s[98:99]
	s_add_u32 s98, s98, 0x6000
	s_addc_u32 s99, s99, 0
	global_load_dword v139, v34, s[98:99]
	s_add_u32 s98, s98, 0x6000
	s_addc_u32 s99, s99, 0
	global_load_dword v140, v34, s[98:99]
	s_add_u32 s98, s98, 0x6000
	s_addc_u32 s99, s99, 0
	global_load_dword v141, v34, s[98:99]
	s_add_u32 s98, s98, 0x6000
	s_addc_u32 s99, s99, 0
	global_load_dword v142, v34, s[98:99]
	s_add_u32 s98, s98, 0x6000
	s_addc_u32 s99, s99, 0
	global_load_dword v143, v34, s[98:99]
	s_add_u32 s98, s98, 0x6000
	s_addc_u32 s99, s99, 0
	global_load_dword v144, v34, s[98:99]
	s_add_u32 s98, s98, 0x6000
	s_addc_u32 s99, s99, 0
	global_load_dword v145, v34, s[98:99]
	s_add_u32 s98, s98, 0x6000
	s_addc_u32 s99, s99, 0
	ds_read_b128 v[18:21], v2 offset:64
	ds_read_b128 v[22:25], v2 offset:80
	ds_read_b128 v[26:29], v2 offset:4160
	ds_read_b128 v[30:33], v2 offset:4176
	s_waitcnt vmcnt(56) lgkmcnt(0)
	v_fmac_f32_e32 v12, v82, v18
	v_fmac_f32_e32 v13, v82, v26
	v_fmac_f32_e32 v12, v83, v19
	v_fmac_f32_e32 v13, v83, v27
	v_fmac_f32_e32 v12, v84, v20
	v_fmac_f32_e32 v13, v84, v28
	v_fmac_f32_e32 v12, v85, v21
	v_fmac_f32_e32 v13, v85, v29
	v_fmac_f32_e32 v12, v86, v22
	v_fmac_f32_e32 v13, v86, v30
	v_fmac_f32_e32 v12, v87, v23
	v_fmac_f32_e32 v13, v87, v31
	v_fmac_f32_e32 v12, v88, v24
	v_fmac_f32_e32 v13, v88, v32
	v_fmac_f32_e32 v12, v89, v25
	v_fmac_f32_e32 v13, v89, v33
	global_load_dword v146, v34, s[98:99]
	s_add_u32 s98, s98, 0x6000
	s_addc_u32 s99, s99, 0
	global_load_dword v147, v34, s[98:99]
	s_add_u32 s98, s98, 0x6000
	s_addc_u32 s99, s99, 0
	global_load_dword v148, v34, s[98:99]
	s_add_u32 s98, s98, 0x6000
	s_addc_u32 s99, s99, 0
	global_load_dword v149, v34, s[98:99]
	s_add_u32 s98, s98, 0x6000
	s_addc_u32 s99, s99, 0
	global_load_dword v150, v34, s[98:99]
	s_add_u32 s98, s98, 0x6000
	s_addc_u32 s99, s99, 0
	global_load_dword v151, v34, s[98:99]
	s_add_u32 s98, s98, 0x6000
	s_addc_u32 s99, s99, 0
	global_load_dword v152, v34, s[98:99]
	s_add_u32 s98, s98, 0x6000
	s_addc_u32 s99, s99, 0
	global_load_dword v153, v34, s[98:99]
	s_add_u32 s98, s98, 0x6000
	s_addc_u32 s99, s99, 0
	ds_read_b128 v[18:21], v2 offset:96
	ds_read_b128 v[22:25], v2 offset:112
	ds_read_b128 v[26:29], v2 offset:4192
	ds_read_b128 v[30:33], v2 offset:4208
	s_waitcnt vmcnt(56) lgkmcnt(0)
	v_fmac_f32_e32 v12, v90, v18
	v_fmac_f32_e32 v13, v90, v26
	v_fmac_f32_e32 v12, v91, v19
	v_fmac_f32_e32 v13, v91, v27
	v_fmac_f32_e32 v12, v92, v20
	v_fmac_f32_e32 v13, v92, v28
	v_fmac_f32_e32 v12, v93, v21
	v_fmac_f32_e32 v13, v93, v29
	v_fmac_f32_e32 v12, v94, v22
	v_fmac_f32_e32 v13, v94, v30
	v_fmac_f32_e32 v12, v95, v23
	v_fmac_f32_e32 v13, v95, v31
	v_fmac_f32_e32 v12, v96, v24
	v_fmac_f32_e32 v13, v96, v32
	v_fmac_f32_e32 v12, v97, v25
	v_fmac_f32_e32 v13, v97, v33
	global_load_dword v154, v34, s[98:99]
	s_add_u32 s98, s98, 0x6000
	s_addc_u32 s99, s99, 0
	global_load_dword v155, v34, s[98:99]
	s_add_u32 s98, s98, 0x6000
	s_addc_u32 s99, s99, 0
	global_load_dword v156, v34, s[98:99]
	s_add_u32 s98, s98, 0x6000
	s_addc_u32 s99, s99, 0
	global_load_dword v157, v34, s[98:99]
	s_add_u32 s98, s98, 0x6000
	s_addc_u32 s99, s99, 0
	global_load_dword v158, v34, s[98:99]
	s_add_u32 s98, s98, 0x6000
	s_addc_u32 s99, s99, 0
	global_load_dword v159, v34, s[98:99]
	s_add_u32 s98, s98, 0x6000
	s_addc_u32 s99, s99, 0
	global_load_dword v160, v34, s[98:99]
	s_add_u32 s98, s98, 0x6000
	s_addc_u32 s99, s99, 0
	global_load_dword v161, v34, s[98:99]
	s_add_u32 s98, s98, 0x6000
	s_addc_u32 s99, s99, 0
	ds_read_b128 v[18:21], v2 offset:128
	ds_read_b128 v[22:25], v2 offset:144
	ds_read_b128 v[26:29], v2 offset:4224
	ds_read_b128 v[30:33], v2 offset:4240
	s_waitcnt vmcnt(56) lgkmcnt(0)
;     ...
; #pragma unroll 8
;         for (int k = ks * 128; k < ks * 128 + 128; ++k) { const float wv = w[(size_t)k * 6144]; a0 += sv[k] * wv; a1 += sv[1024 + k] * wv; }
	v_fmac_f32_e32 v12, v98, v18
	v_fmac_f32_e32 v13, v98, v26
	v_fmac_f32_e32 v12, v99, v19
	v_fmac_f32_e32 v13, v99, v27
	v_fmac_f32_e32 v12, v100, v20
	v_fmac_f32_e32 v13, v100, v28
	v_fmac_f32_e32 v12, v101, v21
	v_fmac_f32_e32 v13, v101, v29
	v_fmac_f32_e32 v12, v102, v22
	v_fmac_f32_e32 v13, v102, v30
	v_fmac_f32_e32 v12, v103, v23
	v_fmac_f32_e32 v13, v103, v31
	v_fmac_f32_e32 v12, v104, v24
	v_fmac_f32_e32 v13, v104, v32
	v_fmac_f32_e32 v12, v105, v25
	v_fmac_f32_e32 v13, v105, v33
	global_load_dword v162, v34, s[98:99]
	s_add_u32 s98, s98, 0x6000
	s_addc_u32 s99, s99, 0
	global_load_dword v163, v34, s[98:99]
	s_add_u32 s98, s98, 0x6000
	s_addc_u32 s99, s99, 0
	global_load_dword v164, v34, s[98:99]
	s_add_u32 s98, s98, 0x6000
	s_addc_u32 s99, s99, 0
	global_load_dword v165, v34, s[98:99]
	s_add_u32 s98, s98, 0x6000
	s_addc_u32 s99, s99, 0
	global_load_dword v166, v34, s[98:99]
	s_add_u32 s98, s98, 0x6000
	s_addc_u32 s99, s99, 0
	global_load_dword v167, v34, s[98:99]
	s_add_u32 s98, s98, 0x6000
	s_addc_u32 s99, s99, 0
	global_load_dword v168, v34, s[98:99]
	s_add_u32 s98, s98, 0x6000
	s_addc_u32 s99, s99, 0
	global_load_dword v169, v34, s[98:99]
	s_add_u32 s98, s98, 0x6000
	s_addc_u32 s99, s99, 0
	ds_read_b128 v[18:21], v2 offset:160
	ds_read_b128 v[22:25], v2 offset:176
	ds_read_b128 v[26:29], v2 offset:4256
	ds_read_b128 v[30:33], v2 offset:4272
	s_waitcnt vmcnt(56) lgkmcnt(0)
	v_fmac_f32_e32 v12, v106, v18
	v_fmac_f32_e32 v13, v106, v26
	v_fmac_f32_e32 v12, v107, v19
	v_fmac_f32_e32 v13, v107, v27
	v_fmac_f32_e32 v12, v108, v20
	v_fmac_f32_e32 v13, v108, v28
	v_fmac_f32_e32 v12, v109, v21
	v_fmac_f32_e32 v13, v109, v29
	v_fmac_f32_e32 v12, v110, v22
	v_fmac_f32_e32 v13, v110, v30
	v_fmac_f32_e32 v12, v111, v23
	v_fmac_f32_e32 v13, v111, v31
	v_fmac_f32_e32 v12, v112, v24
	v_fmac_f32_e32 v13, v112, v32
	v_fmac_f32_e32 v12, v113, v25
	v_fmac_f32_e32 v13, v113, v33
	global_load_dword v170, v34, s[98:99]
	s_add_u32 s98, s98, 0x6000
	s_addc_u32 s99, s99, 0
	global_load_dword v171, v34, s[98:99]
	s_add_u32 s98, s98, 0x6000
	s_addc_u32 s99, s99, 0
	global_load_dword v172, v34, s[98:99]
	s_add_u32 s98, s98, 0x6000
	s_addc_u32 s99, s99, 0
	global_load_dword v173, v34, s[98:99]
	s_add_u32 s98, s98, 0x6000
	s_addc_u32 s99, s99, 0
	global_load_dword v174, v34, s[98:99]
	s_add_u32 s98, s98, 0x6000
	s_addc_u32 s99, s99, 0
	global_load_dword v175, v34, s[98:99]
	s_add_u32 s98, s98, 0x6000
	s_addc_u32 s99, s99, 0
	global_load_dword v176, v34, s[98:99]
	s_add_u32 s98, s98, 0x6000
	s_addc_u32 s99, s99, 0
	global_load_dword v177, v34, s[98:99]
	s_add_u32 s98, s98, 0x6000
	s_addc_u32 s99, s99, 0
	ds_read_b128 v[18:21], v2 offset:192
	ds_read_b128 v[22:25], v2 offset:208
	ds_read_b128 v[26:29], v2 offset:4288
	ds_read_b128 v[30:33], v2 offset:4304
	s_waitcnt vmcnt(56) lgkmcnt(0)
	v_fmac_f32_e32 v12, v114, v18
	v_fmac_f32_e32 v13, v114, v26
	v_fmac_f32_e32 v12, v115, v19
	v_fmac_f32_e32 v13, v115, v27
	v_fmac_f32_e32 v12, v116, v20
	v_fmac_f32_e32 v13, v116, v28
	v_fmac_f32_e32 v12, v117, v21
	v_fmac_f32_e32 v13, v117, v29
	v_fmac_f32_e32 v12, v118, v22
	v_fmac_f32_e32 v13, v118, v30
	v_fmac_f32_e32 v12, v119, v23
	v_fmac_f32_e32 v13, v119, v31
	v_fmac_f32_e32 v12, v120, v24
	v_fmac_f32_e32 v13, v120, v32
	v_fmac_f32_e32 v12, v121, v25
	v_fmac_f32_e32 v13, v121, v33
	global_load_dword v178, v34, s[98:99]
	s_add_u32 s98, s98, 0x6000
	s_addc_u32 s99, s99, 0
	global_load_dword v179, v34, s[98:99]
	s_add_u32 s98, s98, 0x6000
	s_addc_u32 s99, s99, 0
	global_load_dword v180, v34, s[98:99]
	s_add_u32 s98, s98, 0x6000
	s_addc_u32 s99, s99, 0
	global_load_dword v181, v34, s[98:99]
	s_add_u32 s98, s98, 0x6000
	s_addc_u32 s99, s99, 0
	global_load_dword v182, v34, s[98:99]
	s_add_u32 s98, s98, 0x6000
	s_addc_u32 s99, s99, 0
	global_load_dword v183, v34, s[98:99]
	s_add_u32 s98, s98, 0x6000
	s_addc_u32 s99, s99, 0
	global_load_dword v184, v34, s[98:99]
	s_add_u32 s98, s98, 0x6000
	s_addc_u32 s99, s99, 0
	global_load_dword v185, v34, s[98:99]
	s_add_u32 s98, s98, 0x6000
	s_addc_u32 s99, s99, 0
	ds_read_b128 v[18:21], v2 offset:224
	ds_read_b128 v[22:25], v2 offset:240
	ds_read_b128 v[26:29], v2 offset:4320
	ds_read_b128 v[30:33], v2 offset:4336
	s_waitcnt vmcnt(56) lgkmcnt(0)
	v_fmac_f32_e32 v12, v122, v18
	v_fmac_f32_e32 v13, v122, v26
	v_fmac_f32_e32 v12, v123, v19
	v_fmac_f32_e32 v13, v123, v27
	v_fmac_f32_e32 v12, v124, v20
	v_fmac_f32_e32 v13, v124, v28
	v_fmac_f32_e32 v12, v125, v21
	v_fmac_f32_e32 v13, v125, v29
	v_fmac_f32_e32 v12, v126, v22
	v_fmac_f32_e32 v13, v126, v30
	v_fmac_f32_e32 v12, v127, v23
	v_fmac_f32_e32 v13, v127, v31
	v_fmac_f32_e32 v12, v128, v24
	v_fmac_f32_e32 v13, v128, v32
	v_fmac_f32_e32 v12, v129, v25
	v_fmac_f32_e32 v13, v129, v33
	global_load_dword v186, v34, s[98:99]
	s_add_u32 s98, s98, 0x6000
	s_addc_u32 s99, s99, 0
	global_load_dword v187, v34, s[98:99]
	s_add_u32 s98, s98, 0x6000
	s_addc_u32 s99, s99, 0
	global_load_dword v188, v34, s[98:99]
	s_add_u32 s98, s98, 0x6000
	s_addc_u32 s99, s99, 0
	global_load_dword v189, v34, s[98:99]
	s_add_u32 s98, s98, 0x6000
	s_addc_u32 s99, s99, 0
	global_load_dword v190, v34, s[98:99]
	s_add_u32 s98, s98, 0x6000
	s_addc_u32 s99, s99, 0
	global_load_dword v191, v34, s[98:99]
	s_add_u32 s98, s98, 0x6000
	s_addc_u32 s99, s99, 0
	global_load_dword v192, v34, s[98:99]
	s_add_u32 s98, s98, 0x6000
	s_addc_u32 s99, s99, 0
	global_load_dword v193, v34, s[98:99]
	s_add_u32 s98, s98, 0x6000
	s_addc_u32 s99, s99, 0
	ds_read_b128 v[18:21], v2 offset:256
	ds_read_b128 v[22:25], v2 offset:272
	ds_read_b128 v[26:29], v2 offset:4352
	ds_read_b128 v[30:33], v2 offset:4368
	s_waitcnt vmcnt(56) lgkmcnt(0)
;     ...
; #pragma unroll 8
;         for (int k = ks * 128; k < ks * 128 + 128; ++k) { const float wv = w[(size_t)k * 6144]; a0 += sv[k] * wv; a1 += sv[1024 + k] * wv; }
;         red[(ks * 64 + jj) * 2] = a0; red[(ks * 64 + jj) * 2 + 1] = a1;
;         __syncthreads();
;         if (tid < 128) {
;             const int j = tid & 63, wh = tid >> 6;
;             float s = 0.f;
;             for (int q = 0; q < 8; ++q) s += red[(q * 64 + j) * 2 + wh];
;             ((float*)(P.ws + WS_MOD))[(size_t)(layer * 2 + wh) * 6144 + j0 + j] = s + P.in[5][layer * 6144 + j0 + j];
;         }
	v_fmac_f32_e32 v12, v130, v18
	v_fmac_f32_e32 v13, v130, v26
	v_fmac_f32_e32 v12, v131, v19
	v_fmac_f32_e32 v13, v131, v27
	v_fmac_f32_e32 v12, v132, v20
	v_fmac_f32_e32 v13, v132, v28
	v_fmac_f32_e32 v12, v133, v21
	v_fmac_f32_e32 v13, v133, v29
	v_fmac_f32_e32 v12, v134, v22
	v_fmac_f32_e32 v13, v134, v30
	v_fmac_f32_e32 v12, v135, v23
	v_fmac_f32_e32 v13, v135, v31
	v_fmac_f32_e32 v12, v136, v24
	v_fmac_f32_e32 v13, v136, v32
	v_fmac_f32_e32 v12, v137, v25
	v_fmac_f32_e32 v13, v137, v33
	ds_read_b128 v[18:21], v2 offset:288
	ds_read_b128 v[22:25], v2 offset:304
	ds_read_b128 v[26:29], v2 offset:4384
	ds_read_b128 v[30:33], v2 offset:4400
	s_waitcnt vmcnt(48) lgkmcnt(0)
	v_fmac_f32_e32 v12, v138, v18
	v_fmac_f32_e32 v13, v138, v26
	v_fmac_f32_e32 v12, v139, v19
	v_fmac_f32_e32 v13, v139, v27
	v_fmac_f32_e32 v12, v140, v20
	v_fmac_f32_e32 v13, v140, v28
	v_fmac_f32_e32 v12, v141, v21
	v_fmac_f32_e32 v13, v141, v29
	v_fmac_f32_e32 v12, v142, v22
	v_fmac_f32_e32 v13, v142, v30
	v_fmac_f32_e32 v12, v143, v23
	v_fmac_f32_e32 v13, v143, v31
	v_fmac_f32_e32 v12, v144, v24
	v_fmac_f32_e32 v13, v144, v32
	v_fmac_f32_e32 v12, v145, v25
	v_fmac_f32_e32 v13, v145, v33
	ds_read_b128 v[18:21], v2 offset:320
	ds_read_b128 v[22:25], v2 offset:336
	ds_read_b128 v[26:29], v2 offset:4416
	ds_read_b128 v[30:33], v2 offset:4432
	s_waitcnt vmcnt(40) lgkmcnt(0)
	v_fmac_f32_e32 v12, v146, v18
	v_fmac_f32_e32 v13, v146, v26
	v_fmac_f32_e32 v12, v147, v19
	v_fmac_f32_e32 v13, v147, v27
	v_fmac_f32_e32 v12, v148, v20
	v_fmac_f32_e32 v13, v148, v28
	v_fmac_f32_e32 v12, v149, v21
	v_fmac_f32_e32 v13, v149, v29
	v_fmac_f32_e32 v12, v150, v22
	v_fmac_f32_e32 v13, v150, v30
	v_fmac_f32_e32 v12, v151, v23
	v_fmac_f32_e32 v13, v151, v31
	v_fmac_f32_e32 v12, v152, v24
	v_fmac_f32_e32 v13, v152, v32
	v_fmac_f32_e32 v12, v153, v25
	v_fmac_f32_e32 v13, v153, v33
	ds_read_b128 v[18:21], v2 offset:352
	ds_read_b128 v[22:25], v2 offset:368
	ds_read_b128 v[26:29], v2 offset:4448
	ds_read_b128 v[30:33], v2 offset:4464
	s_waitcnt vmcnt(32) lgkmcnt(0)
	v_fmac_f32_e32 v12, v154, v18
	v_fmac_f32_e32 v13, v154, v26
	v_fmac_f32_e32 v12, v155, v19
	v_fmac_f32_e32 v13, v155, v27
	v_fmac_f32_e32 v12, v156, v20
	v_fmac_f32_e32 v13, v156, v28
	v_fmac_f32_e32 v12, v157, v21
	v_fmac_f32_e32 v13, v157, v29
	v_fmac_f32_e32 v12, v158, v22
	v_fmac_f32_e32 v13, v158, v30
	v_fmac_f32_e32 v12, v159, v23
	v_fmac_f32_e32 v13, v159, v31
	v_fmac_f32_e32 v12, v160, v24
	v_fmac_f32_e32 v13, v160, v32
	v_fmac_f32_e32 v12, v161, v25
	v_fmac_f32_e32 v13, v161, v33
	ds_read_b128 v[18:21], v2 offset:384
	ds_read_b128 v[22:25], v2 offset:400
	ds_read_b128 v[26:29], v2 offset:4480
	ds_read_b128 v[30:33], v2 offset:4496
	s_waitcnt vmcnt(24) lgkmcnt(0)
	v_fmac_f32_e32 v12, v162, v18
	v_fmac_f32_e32 v13, v162, v26
	v_fmac_f32_e32 v12, v163, v19
	v_fmac_f32_e32 v13, v163, v27
	v_fmac_f32_e32 v12, v164, v20
	v_fmac_f32_e32 v13, v164, v28
	v_fmac_f32_e32 v12, v165, v21
	v_fmac_f32_e32 v13, v165, v29
	v_fmac_f32_e32 v12, v166, v22
	v_fmac_f32_e32 v13, v166, v30
	v_fmac_f32_e32 v12, v167, v23
	v_fmac_f32_e32 v13, v167, v31
	v_fmac_f32_e32 v12, v168, v24
	v_fmac_f32_e32 v13, v168, v32
	v_fmac_f32_e32 v12, v169, v25
	v_fmac_f32_e32 v13, v169, v33
	ds_read_b128 v[18:21], v2 offset:416
	ds_read_b128 v[22:25], v2 offset:432
	ds_read_b128 v[26:29], v2 offset:4512
	ds_read_b128 v[30:33], v2 offset:4528
	s_waitcnt vmcnt(16) lgkmcnt(0)
	v_fmac_f32_e32 v12, v170, v18
	v_fmac_f32_e32 v13, v170, v26
	v_fmac_f32_e32 v12, v171, v19
	v_fmac_f32_e32 v13, v171, v27
	v_fmac_f32_e32 v12, v172, v20
	v_fmac_f32_e32 v13, v172, v28
	v_fmac_f32_e32 v12, v173, v21
	v_fmac_f32_e32 v13, v173, v29
	v_fmac_f32_e32 v12, v174, v22
	v_fmac_f32_e32 v13, v174, v30
	v_fmac_f32_e32 v12, v175, v23
	v_fmac_f32_e32 v13, v175, v31
	v_fmac_f32_e32 v12, v176, v24
	v_fmac_f32_e32 v13, v176, v32
	v_fmac_f32_e32 v12, v177, v25
	v_fmac_f32_e32 v13, v177, v33
	ds_read_b128 v[18:21], v2 offset:448
	ds_read_b128 v[22:25], v2 offset:464
	ds_read_b128 v[26:29], v2 offset:4544
	ds_read_b128 v[30:33], v2 offset:4560
	s_waitcnt vmcnt(8) lgkmcnt(0)
	v_fmac_f32_e32 v12, v178, v18
	v_fmac_f32_e32 v13, v178, v26
	v_fmac_f32_e32 v12, v179, v19
	v_fmac_f32_e32 v13, v179, v27
	v_fmac_f32_e32 v12, v180, v20
	v_fmac_f32_e32 v13, v180, v28
	v_fmac_f32_e32 v12, v181, v21
	v_fmac_f32_e32 v13, v181, v29
	v_fmac_f32_e32 v12, v182, v22
	v_fmac_f32_e32 v13, v182, v30
	v_fmac_f32_e32 v12, v183, v23
	v_fmac_f32_e32 v13, v183, v31
	v_fmac_f32_e32 v12, v184, v24
	v_fmac_f32_e32 v13, v184, v32
	v_fmac_f32_e32 v12, v185, v25
	v_fmac_f32_e32 v13, v185, v33
	ds_read_b128 v[18:21], v2 offset:480
	ds_read_b128 v[22:25], v2 offset:496
	ds_read_b128 v[26:29], v2 offset:4576
	ds_read_b128 v[30:33], v2 offset:4592
	s_waitcnt vmcnt(0) lgkmcnt(0)
	v_fmac_f32_e32 v12, v186, v18
	v_fmac_f32_e32 v13, v186, v26
	v_fmac_f32_e32 v12, v187, v19
	v_fmac_f32_e32 v13, v187, v27
	v_fmac_f32_e32 v12, v188, v20
	v_fmac_f32_e32 v13, v188, v28
	v_fmac_f32_e32 v12, v189, v21
	v_fmac_f32_e32 v13, v189, v29
	v_fmac_f32_e32 v12, v190, v22
	v_fmac_f32_e32 v13, v190, v30
	v_fmac_f32_e32 v12, v191, v23
	v_fmac_f32_e32 v13, v191, v31
	v_fmac_f32_e32 v12, v192, v24
	v_fmac_f32_e32 v13, v192, v32
	v_fmac_f32_e32 v12, v193, v25
	v_fmac_f32_e32 v13, v193, v33
	v_add_u32_e32 v2, 0, v65
	ds_write_b64 v2, v[12:13] offset:8208
	s_waitcnt lgkmcnt(0)
	s_barrier
	s_and_saveexec_b64 s[0:1], s[6:7]
	s_cbranch_execz .LBB0_8
	s_mul_i32 s10, s14, 0x1800
	s_add_i32 s10, s10, s8
	v_or_b32_e32 v10, s10, v202
	v_readlane_b32 s16, v253, 19
	v_ashrrev_i32_e32 v11, 31, v10
	v_readlane_b32 s26, v253, 29
	v_readlane_b32 s27, v253, 30
	v_add_u32_e32 v22, 16, v14
	v_lshl_or_b32 v24, s14, 1, v1
	v_lshl_add_u64 v[10:11], v[10:11], 2, s[26:27]
	global_load_dword v17, v[10:11], off
	ds_read2st64_b32 v[12:13], v22 offset0:32 offset1:34
	ds_read2st64_b32 v[18:19], v22 offset0:36 offset1:38
	ds_read2st64_b32 v[20:21], v22 offset0:40 offset1:42
	ds_read2st64_b32 v[22:23], v22 offset0:44 offset1:46
	v_mov_b64_e32 v[10:11], s[2:3]
	s_waitcnt lgkmcnt(3)
	v_add_f32_e32 v12, 0, v12
	v_add_f32_e32 v12, v12, v13
	s_waitcnt lgkmcnt(2)
	v_add_f32_e32 v12, v12, v18
	v_add_f32_e32 v12, v12, v19
	s_waitcnt lgkmcnt(1)
	v_add_f32_e32 v12, v12, v20
	v_add_f32_e32 v12, v12, v21
	v_mad_i64_i32 v[10:11], s[10:11], v24, s12, v[10:11]
	s_waitcnt lgkmcnt(0)
	v_add_f32_e32 v12, v12, v22
	v_lshlrev_b32_e32 v2, 2, v202
	v_lshl_add_u64 v[10:11], s[8:9], 2, v[10:11]
	v_add_f32_e32 v12, v12, v23
	v_lshl_add_u64 v[10:11], v[10:11], 0, v[2:3]
	v_readlane_b32 s17, v253, 20
	v_readlane_b32 s18, v253, 21
	v_readlane_b32 s19, v253, 22
	v_readlane_b32 s20, v253, 23
	v_readlane_b32 s21, v253, 24
	v_readlane_b32 s22, v253, 25
	v_readlane_b32 s23, v253, 26
	v_readlane_b32 s24, v253, 27
	v_readlane_b32 s25, v253, 28
	v_readlane_b32 s28, v253, 31
	v_readlane_b32 s29, v253, 32
	v_readlane_b32 s30, v253, 33
	v_readlane_b32 s31, v253, 34
	s_waitcnt vmcnt(0)
	v_add_f32_e32 v12, v12, v17
	global_store_dword v[10:11], v12, off
	s_branch .LBB0_8
